# diff-attention: one address computation for both K half reads of a QK step
# speedup vs baseline: 1.0000x; 1.0000x over previous
.Lattn_noresc0_a:
	ds_read_b64_tr_b16 v[156:157], v215 offset:36864
	ds_read_b64_tr_b16 v[158:159], v215 offset:38912
	ds_read_b64_tr_b16 v[192:193], v212 offset:40960
	ds_read_b64_tr_b16 v[194:195], v212 offset:43008
	ds_read_b64_tr_b16 v[196:197], v213 offset:40960
	ds_read_b64_tr_b16 v[198:199], v213 offset:43008
	ds_read_b64_tr_b16 v[200:201], v214 offset:40960
	ds_read_b64_tr_b16 v[202:203], v214 offset:43008
	v_sub_f32_e32 v160, v160, v229
	v_sub_f32_e32 v161, v161, v229
	v_sub_f32_e32 v162, v162, v229
	s_waitcnt lgkmcnt(12)
	v_mfma_f32_32x32x16_bf16 v[112:127], v[132:135], v[144:147], v[112:127]
	ds_read_b64_tr_b16 v[204:205], v215 offset:40960
	ds_read_b64_tr_b16 v[206:207], v215 offset:43008
	v_sub_f32_e32 v163, v163, v229
	v_exp_f32_e32 v160, v160
	v_exp_f32_e32 v161, v161
	v_exp_f32_e32 v162, v162
	v_exp_f32_e32 v163, v163
	s_waitcnt lgkmcnt(12)
	v_mfma_f32_32x32x16_bf16 v[96:111], v[132:135], v[148:151], v[96:111]
	ds_read_b64_tr_b16 v[144:145], v212 offset:45056
	ds_read_b64_tr_b16 v[146:147], v212 offset:47104
	v_add_f32_e32 v254, v160, v161
	v_add_f32_e32 v254, v254, v162
	v_add_f32_e32 v254, v254, v163
	v_sub_f32_e32 v164, v164, v229
	v_sub_f32_e32 v165, v165, v229
	s_waitcnt lgkmcnt(12)
	v_mfma_f32_32x32x16_bf16 v[80:95], v[132:135], v[152:155], v[80:95]
	ds_read_b64_tr_b16 v[148:149], v213 offset:45056
	ds_read_b64_tr_b16 v[150:151], v213 offset:47104
	v_sub_f32_e32 v166, v166, v229
	v_sub_f32_e32 v167, v167, v229
	v_exp_f32_e32 v164, v164
	v_exp_f32_e32 v165, v165
	v_exp_f32_e32 v166, v166
	s_waitcnt lgkmcnt(12)
	v_mfma_f32_32x32x16_bf16 v[48:63], v[132:135], v[156:159], v[48:63]
	ds_read_b64_tr_b16 v[152:153], v214 offset:45056
	ds_read_b64_tr_b16 v[154:155], v214 offset:47104
	v_exp_f32_e32 v167, v167
	v_add_f32_e32 v254, v254, v164
	v_add_f32_e32 v254, v254, v165
	v_add_f32_e32 v254, v254, v166
	v_add_f32_e32 v254, v254, v167
	s_waitcnt lgkmcnt(12)
	v_mfma_f32_32x32x16_bf16 v[112:127], v[136:139], v[192:195], v[112:127]
	ds_read_b64_tr_b16 v[156:157], v215 offset:45056
	ds_read_b64_tr_b16 v[158:159], v215 offset:47104
	v_cvt_pk_bf16_f32 v160, v160, v161
	v_cvt_pk_bf16_f32 v161, v162, v163
	v_sub_f32_e32 v168, v168, v229
	v_sub_f32_e32 v169, v169, v229
	v_sub_f32_e32 v170, v170, v229
	s_waitcnt lgkmcnt(12)
	v_mfma_f32_32x32x16_bf16 v[96:111], v[136:139], v[196:199], v[96:111]
	v_add_u32_e32 v230, v236, v244
	ds_read_b128 v[192:195], v230
	v_sub_f32_e32 v171, v171, v229
	v_exp_f32_e32 v168, v168
	v_exp_f32_e32 v169, v169
	v_exp_f32_e32 v170, v170
	v_exp_f32_e32 v171, v171
	s_waitcnt lgkmcnt(11)
	v_mfma_f32_32x32x16_bf16 v[80:95], v[136:139], v[200:203], v[80:95]
	v_add3_u32 v230, v237, v244, s48
	ds_read_b128 v[196:199], v230
	ds_read_b128 v[200:203], v230 offset:8192
	v_add_f32_e32 v254, v254, v168
	v_add_f32_e32 v254, v254, v169
	v_add_f32_e32 v254, v254, v170
	v_add_f32_e32 v254, v254, v171
	v_cvt_pk_bf16_f32 v162, v164, v165
	s_waitcnt lgkmcnt(11)
	v_mfma_f32_32x32x16_bf16 v[48:63], v[136:139], v[204:207], v[48:63]
	v_cvt_pk_bf16_f32 v163, v166, v167
	v_sub_f32_e32 v172, v172, v229
	v_sub_f32_e32 v173, v173, v229
	v_sub_f32_e32 v174, v174, v229
	v_sub_f32_e32 v175, v175, v229
	s_waitcnt lgkmcnt(9)
	v_mfma_f32_32x32x16_bf16 v[112:127], v[140:143], v[144:147], v[112:127]
	v_add_u32_e32 v230, v236, v245
	ds_read_b128 v[204:207], v230
	v_exp_f32_e32 v172, v172
	v_exp_f32_e32 v173, v173
	v_exp_f32_e32 v174, v174
	v_exp_f32_e32 v175, v175
	v_add_f32_e32 v254, v254, v172
	s_waitcnt lgkmcnt(8)
	v_mfma_f32_32x32x16_bf16 v[96:111], v[140:143], v[148:151], v[96:111]
	v_add_f32_e32 v254, v254, v173
	v_add_f32_e32 v254, v254, v174
	v_add_f32_e32 v254, v254, v175
	v_cvt_pk_bf16_f32 v164, v168, v169
	v_cvt_pk_bf16_f32 v165, v170, v171
	s_waitcnt lgkmcnt(6)
	v_mfma_f32_32x32x16_bf16 v[80:95], v[140:143], v[152:155], v[80:95]
	v_sub_f32_e32 v176, v176, v229
	v_sub_f32_e32 v177, v177, v229
	v_sub_f32_e32 v178, v178, v229
	v_sub_f32_e32 v179, v179, v229
	v_exp_f32_e32 v176, v176
	v_exp_f32_e32 v177, v177
	s_waitcnt lgkmcnt(4)
	v_mfma_f32_32x32x16_bf16 v[48:63], v[140:143], v[156:159], v[48:63]
	v_exp_f32_e32 v178, v178
	v_exp_f32_e32 v179, v179
	v_add_f32_e32 v255, v176, v177
	v_add_f32_e32 v255, v255, v178
	v_add_f32_e32 v255, v255, v179
	s_waitcnt lgkmcnt(2)
	v_mfma_f32_32x32x16_bf16 v[128:143], v[196:199], v[192:195], 0
	v_cvt_pk_bf16_f32 v166, v172, v173
	v_cvt_pk_bf16_f32 v167, v174, v175
	v_sub_f32_e32 v180, v180, v229
	v_sub_f32_e32 v181, v181, v229
	v_sub_f32_e32 v182, v182, v229
	s_waitcnt lgkmcnt(1)
	v_mfma_f32_32x32x16_bf16 v[144:159], v[200:203], v[192:195], 0
	v_add3_u32 v230, v237, v245, s48
	ds_read_b128 v[196:199], v230
	ds_read_b128 v[200:203], v230 offset:8192
	v_add_u32_e32 v230, v236, v246
	ds_read_b128 v[192:195], v230
	v_sub_f32_e32 v183, v183, v229
	v_exp_f32_e32 v180, v180
	v_exp_f32_e32 v181, v181
	v_exp_f32_e32 v182, v182
	v_exp_f32_e32 v183, v183
	s_waitcnt lgkmcnt(2)
	v_mfma_f32_32x32x16_bf16 v[128:143], v[196:199], v[204:207], v[128:143]
	v_add_f32_e32 v255, v255, v180
	v_add_f32_e32 v255, v255, v181
	v_add_f32_e32 v255, v255, v182
	v_add_f32_e32 v255, v255, v183
	v_cvt_pk_bf16_f32 v168, v176, v177
	s_waitcnt lgkmcnt(1)
	v_mfma_f32_32x32x16_bf16 v[144:159], v[200:203], v[204:207], v[144:159]
	v_add3_u32 v230, v237, v246, s48
	ds_read_b128 v[196:199], v230
	ds_read_b128 v[200:203], v230 offset:8192
	v_add_u32_e32 v230, v236, v247
	ds_read_b128 v[204:207], v230
	v_cvt_pk_bf16_f32 v169, v178, v179
	v_sub_f32_e32 v184, v184, v229
	v_sub_f32_e32 v185, v185, v229
	v_sub_f32_e32 v186, v186, v229
	v_sub_f32_e32 v187, v187, v229
	s_waitcnt lgkmcnt(2)
	v_mfma_f32_32x32x16_bf16 v[128:143], v[196:199], v[192:195], v[128:143]
	v_exp_f32_e32 v184, v184
	v_exp_f32_e32 v185, v185
	v_exp_f32_e32 v186, v186
	v_exp_f32_e32 v187, v187
	v_add_f32_e32 v255, v255, v184
	s_waitcnt lgkmcnt(1)
	v_mfma_f32_32x32x16_bf16 v[144:159], v[200:203], v[192:195], v[144:159]
	v_add3_u32 v230, v237, v247, s48
	ds_read_b128 v[196:199], v230
	ds_read_b128 v[200:203], v230 offset:8192
	v_add_f32_e32 v255, v255, v185
	v_add_f32_e32 v255, v255, v186
	v_add_f32_e32 v255, v255, v187
	v_cvt_pk_bf16_f32 v170, v180, v181
	v_cvt_pk_bf16_f32 v171, v182, v183
	s_waitcnt lgkmcnt(1)
	v_mfma_f32_32x32x16_bf16 v[128:143], v[196:199], v[204:207], v[128:143]
	v_sub_f32_e32 v188, v188, v229
	v_sub_f32_e32 v189, v189, v229
	v_sub_f32_e32 v190, v190, v229
	v_sub_f32_e32 v191, v191, v229
	v_exp_f32_e32 v188, v188
	s_waitcnt lgkmcnt(0)
	v_mfma_f32_32x32x16_bf16 v[144:159], v[200:203], v[204:207], v[144:159]
	v_exp_f32_e32 v189, v189
	v_exp_f32_e32 v190, v190
	v_exp_f32_e32 v191, v191
	v_add_f32_e32 v255, v255, v188
	v_add_f32_e32 v255, v255, v189
	v_add_f32_e32 v255, v255, v190
	v_add_f32_e32 v255, v255, v191
	v_cvt_pk_bf16_f32 v172, v184, v185
	v_cvt_pk_bf16_f32 v173, v186, v187
	v_cvt_pk_bf16_f32 v174, v188, v189
	v_cvt_pk_bf16_f32 v175, v190, v191
	v_add_f32_e32 v254, v254, v255
	v_mov_b32_e32 v255, v254
	s_nop 1
	v_permlane32_swap_b32_e32 v254, v255
	v_add_f32_e32 v254, v254, v255
	v_fma_f32 v251, v251, v228, v254
	s_branch .Lattn_mid

.Lattn_noresc0_b:
	v_add_u32_e32 v230, v236, v244
	ds_read_b128 v[192:195], v230
	v_add3_u32 v230, v237, v244, s48
	ds_read_b128 v[196:199], v230
	ds_read_b128 v[200:203], v230 offset:8192
	v_add_u32_e32 v230, v236, v245
	ds_read_b128 v[204:207], v230
	v_sub_f32_e32 v160, v160, v229
	v_sub_f32_e32 v161, v161, v229
	v_sub_f32_e32 v162, v162, v229
	s_waitcnt lgkmcnt(2)
	v_mfma_f32_32x32x16_bf16 v[128:143], v[196:199], v[192:195], 0
	v_sub_f32_e32 v163, v163, v229
	v_exp_f32_e32 v160, v160
	v_exp_f32_e32 v161, v161
	v_exp_f32_e32 v162, v162
	v_exp_f32_e32 v163, v163
	v_add_f32_e32 v254, v160, v161
	v_add_f32_e32 v254, v254, v162
	v_add_f32_e32 v254, v254, v163
	v_sub_f32_e32 v164, v164, v229
	v_sub_f32_e32 v165, v165, v229
	v_sub_f32_e32 v166, v166, v229
	v_sub_f32_e32 v167, v167, v229
	v_exp_f32_e32 v164, v164
	s_waitcnt lgkmcnt(1)
	v_mfma_f32_32x32x16_bf16 v[144:159], v[200:203], v[192:195], 0
	v_add3_u32 v230, v237, v245, s48
	ds_read_b128 v[196:199], v230
	ds_read_b128 v[200:203], v230 offset:8192
	v_add_u32_e32 v230, v236, v246
	ds_read_b128 v[192:195], v230
	v_exp_f32_e32 v165, v165
	v_exp_f32_e32 v166, v166
	v_exp_f32_e32 v167, v167
	v_add_f32_e32 v254, v254, v164
	v_add_f32_e32 v254, v254, v165
	v_add_f32_e32 v254, v254, v166
	v_add_f32_e32 v254, v254, v167
	v_cvt_pk_bf16_f32 v160, v160, v161
	v_cvt_pk_bf16_f32 v161, v162, v163
	v_sub_f32_e32 v168, v168, v229
	v_sub_f32_e32 v169, v169, v229
	v_sub_f32_e32 v170, v170, v229
	v_sub_f32_e32 v171, v171, v229
	v_exp_f32_e32 v168, v168
	s_waitcnt lgkmcnt(2)
	v_mfma_f32_32x32x16_bf16 v[128:143], v[196:199], v[204:207], v[128:143]
	v_exp_f32_e32 v169, v169
	v_exp_f32_e32 v170, v170
	v_exp_f32_e32 v171, v171
	v_add_f32_e32 v254, v254, v168
	v_add_f32_e32 v254, v254, v169
	v_add_f32_e32 v254, v254, v170
	v_add_f32_e32 v254, v254, v171
	v_cvt_pk_bf16_f32 v162, v164, v165
	v_cvt_pk_bf16_f32 v163, v166, v167
	v_sub_f32_e32 v172, v172, v229
	v_sub_f32_e32 v173, v173, v229
	v_sub_f32_e32 v174, v174, v229
	v_sub_f32_e32 v175, v175, v229
	v_exp_f32_e32 v172, v172
	s_waitcnt lgkmcnt(1)
	v_mfma_f32_32x32x16_bf16 v[144:159], v[200:203], v[204:207], v[144:159]
	v_add3_u32 v230, v237, v246, s48
	ds_read_b128 v[196:199], v230
	ds_read_b128 v[200:203], v230 offset:8192
	v_add_u32_e32 v230, v236, v247
	ds_read_b128 v[204:207], v230
	v_exp_f32_e32 v173, v173
	v_exp_f32_e32 v174, v174
	v_exp_f32_e32 v175, v175
	v_add_f32_e32 v254, v254, v172
	v_add_f32_e32 v254, v254, v173
	v_add_f32_e32 v254, v254, v174
	v_add_f32_e32 v254, v254, v175
	v_cvt_pk_bf16_f32 v164, v168, v169
	v_cvt_pk_bf16_f32 v165, v170, v171
	v_sub_f32_e32 v176, v176, v229
	v_sub_f32_e32 v177, v177, v229
	v_sub_f32_e32 v178, v178, v229
	v_sub_f32_e32 v179, v179, v229
	v_exp_f32_e32 v176, v176
	s_waitcnt lgkmcnt(2)
	v_mfma_f32_32x32x16_bf16 v[128:143], v[196:199], v[192:195], v[128:143]
	v_exp_f32_e32 v177, v177
	v_exp_f32_e32 v178, v178
	v_exp_f32_e32 v179, v179
	v_add_f32_e32 v255, v176, v177
	v_add_f32_e32 v255, v255, v178
	v_add_f32_e32 v255, v255, v179
	v_cvt_pk_bf16_f32 v166, v172, v173
	v_cvt_pk_bf16_f32 v167, v174, v175
	v_sub_f32_e32 v180, v180, v229
	v_sub_f32_e32 v181, v181, v229
	v_sub_f32_e32 v182, v182, v229
	v_sub_f32_e32 v183, v183, v229
	v_exp_f32_e32 v180, v180
	v_exp_f32_e32 v181, v181
	s_waitcnt lgkmcnt(1)
	v_mfma_f32_32x32x16_bf16 v[144:159], v[200:203], v[192:195], v[144:159]
	v_add3_u32 v230, v237, v247, s48
	ds_read_b128 v[196:199], v230
	ds_read_b128 v[200:203], v230 offset:8192
	v_exp_f32_e32 v182, v182
	v_exp_f32_e32 v183, v183
	v_add_f32_e32 v255, v255, v180
	v_add_f32_e32 v255, v255, v181
	v_add_f32_e32 v255, v255, v182
	v_add_f32_e32 v255, v255, v183
	v_cvt_pk_bf16_f32 v168, v176, v177
	v_cvt_pk_bf16_f32 v169, v178, v179
	v_sub_f32_e32 v184, v184, v229
	v_sub_f32_e32 v185, v185, v229
	v_sub_f32_e32 v186, v186, v229
	v_sub_f32_e32 v187, v187, v229
	v_exp_f32_e32 v184, v184
	s_waitcnt lgkmcnt(1)
	v_mfma_f32_32x32x16_bf16 v[128:143], v[196:199], v[204:207], v[128:143]
	v_exp_f32_e32 v185, v185
	v_exp_f32_e32 v186, v186
	v_exp_f32_e32 v187, v187
	v_add_f32_e32 v255, v255, v184
	v_add_f32_e32 v255, v255, v185
	v_add_f32_e32 v255, v255, v186
	v_add_f32_e32 v255, v255, v187
	v_cvt_pk_bf16_f32 v170, v180, v181
	v_cvt_pk_bf16_f32 v171, v182, v183
	v_sub_f32_e32 v188, v188, v229
	v_sub_f32_e32 v189, v189, v229
	v_sub_f32_e32 v190, v190, v229
	v_sub_f32_e32 v191, v191, v229
	v_exp_f32_e32 v188, v188
	s_waitcnt lgkmcnt(0)
	v_mfma_f32_32x32x16_bf16 v[144:159], v[200:203], v[204:207], v[144:159]
	v_exp_f32_e32 v189, v189
	v_exp_f32_e32 v190, v190
	v_exp_f32_e32 v191, v191
	v_add_f32_e32 v255, v255, v188
	v_add_f32_e32 v255, v255, v189
	v_add_f32_e32 v255, v255, v190
	v_add_f32_e32 v255, v255, v191
	v_cvt_pk_bf16_f32 v172, v184, v185
	v_cvt_pk_bf16_f32 v173, v186, v187
	v_cvt_pk_bf16_f32 v174, v188, v189
	v_cvt_pk_bf16_f32 v175, v190, v191
	v_add_f32_e32 v254, v254, v255
	v_mov_b32_e32 v255, v254
	s_nop 1
	v_permlane32_swap_b32_e32 v254, v255
	v_add_f32_e32 v254, v254, v255
	v_fma_f32 v251, v251, v228, v254
	s_branch .Lattn_mid

.Lattn_noresc1_c:
	ds_read_b64_tr_b16 v[188:189], v215 offset:36864
	ds_read_b64_tr_b16 v[190:191], v215 offset:38912
	ds_read_b64_tr_b16 v[192:193], v212 offset:40960
	ds_read_b64_tr_b16 v[194:195], v212 offset:43008
	ds_read_b64_tr_b16 v[196:197], v213 offset:40960
	ds_read_b64_tr_b16 v[198:199], v213 offset:43008
	ds_read_b64_tr_b16 v[200:201], v214 offset:40960
	ds_read_b64_tr_b16 v[202:203], v214 offset:43008
	v_sub_f32_e32 v128, v128, v229
	v_sub_f32_e32 v129, v129, v229
	v_sub_f32_e32 v130, v130, v229
	s_waitcnt lgkmcnt(12)
	v_mfma_f32_32x32x16_bf16 v[64:79], v[164:167], v[176:179], v[64:79]
	ds_read_b64_tr_b16 v[204:205], v215 offset:40960
	ds_read_b64_tr_b16 v[206:207], v215 offset:43008
	v_sub_f32_e32 v131, v131, v229
	v_exp_f32_e32 v128, v128
	v_exp_f32_e32 v129, v129
	v_exp_f32_e32 v130, v130
	v_exp_f32_e32 v131, v131
	s_waitcnt lgkmcnt(12)
	v_mfma_f32_32x32x16_bf16 v[32:47], v[164:167], v[180:183], v[32:47]
	ds_read_b64_tr_b16 v[176:177], v212 offset:45056
	ds_read_b64_tr_b16 v[178:179], v212 offset:47104
	v_add_f32_e32 v254, v128, v129
	v_add_f32_e32 v254, v254, v130
	v_add_f32_e32 v254, v254, v131
	v_sub_f32_e32 v132, v132, v229
	v_sub_f32_e32 v133, v133, v229
	s_waitcnt lgkmcnt(12)
	v_mfma_f32_32x32x16_bf16 v[16:31], v[164:167], v[184:187], v[16:31]
	ds_read_b64_tr_b16 v[180:181], v213 offset:45056
	ds_read_b64_tr_b16 v[182:183], v213 offset:47104
	v_sub_f32_e32 v134, v134, v229
	v_sub_f32_e32 v135, v135, v229
	v_exp_f32_e32 v132, v132
	v_exp_f32_e32 v133, v133
	v_exp_f32_e32 v134, v134
	s_waitcnt lgkmcnt(12)
	v_mfma_f32_32x32x16_bf16 v[0:15], v[164:167], v[188:191], v[0:15]
	ds_read_b64_tr_b16 v[184:185], v214 offset:45056
	ds_read_b64_tr_b16 v[186:187], v214 offset:47104
	v_exp_f32_e32 v135, v135
	v_add_f32_e32 v254, v254, v132
	v_add_f32_e32 v254, v254, v133
	v_add_f32_e32 v254, v254, v134
	v_add_f32_e32 v254, v254, v135
	s_waitcnt lgkmcnt(12)
	v_mfma_f32_32x32x16_bf16 v[64:79], v[168:171], v[192:195], v[64:79]
	ds_read_b64_tr_b16 v[188:189], v215 offset:45056
	ds_read_b64_tr_b16 v[190:191], v215 offset:47104
	v_cvt_pk_bf16_f32 v128, v128, v129
	v_cvt_pk_bf16_f32 v129, v130, v131
	v_sub_f32_e32 v136, v136, v229
	v_sub_f32_e32 v137, v137, v229
	v_sub_f32_e32 v138, v138, v229
	s_waitcnt lgkmcnt(12)
	v_mfma_f32_32x32x16_bf16 v[32:47], v[168:171], v[196:199], v[32:47]
	v_add_u32_e32 v230, v236, v240
	ds_read_b128 v[192:195], v230
	v_sub_f32_e32 v139, v139, v229
	v_exp_f32_e32 v136, v136
	v_exp_f32_e32 v137, v137
	v_exp_f32_e32 v138, v138
	v_exp_f32_e32 v139, v139
	s_waitcnt lgkmcnt(11)
	v_mfma_f32_32x32x16_bf16 v[16:31], v[168:171], v[200:203], v[16:31]
	v_add3_u32 v230, v237, v240, s51
	ds_read_b128 v[196:199], v230
	ds_read_b128 v[200:203], v230 offset:8192
	v_add_f32_e32 v254, v254, v136
	v_add_f32_e32 v254, v254, v137
	v_add_f32_e32 v254, v254, v138
	v_add_f32_e32 v254, v254, v139
	v_cvt_pk_bf16_f32 v130, v132, v133
	s_waitcnt lgkmcnt(11)
	v_mfma_f32_32x32x16_bf16 v[0:15], v[168:171], v[204:207], v[0:15]
	v_cvt_pk_bf16_f32 v131, v134, v135
	v_sub_f32_e32 v140, v140, v229
	v_sub_f32_e32 v141, v141, v229
	v_sub_f32_e32 v142, v142, v229
	v_sub_f32_e32 v143, v143, v229
	s_waitcnt lgkmcnt(9)
	v_mfma_f32_32x32x16_bf16 v[64:79], v[172:175], v[176:179], v[64:79]
	v_add_u32_e32 v230, v236, v241
	ds_read_b128 v[204:207], v230
	v_exp_f32_e32 v140, v140
	v_exp_f32_e32 v141, v141
	v_exp_f32_e32 v142, v142
	v_exp_f32_e32 v143, v143
	v_add_f32_e32 v254, v254, v140
	s_waitcnt lgkmcnt(8)
	v_mfma_f32_32x32x16_bf16 v[32:47], v[172:175], v[180:183], v[32:47]
	v_add_f32_e32 v254, v254, v141
	v_add_f32_e32 v254, v254, v142
	v_add_f32_e32 v254, v254, v143
	v_cvt_pk_bf16_f32 v132, v136, v137
	v_cvt_pk_bf16_f32 v133, v138, v139
	s_waitcnt lgkmcnt(6)
	v_mfma_f32_32x32x16_bf16 v[16:31], v[172:175], v[184:187], v[16:31]
	v_sub_f32_e32 v144, v144, v229
	v_sub_f32_e32 v145, v145, v229
	v_sub_f32_e32 v146, v146, v229
	v_sub_f32_e32 v147, v147, v229
	v_exp_f32_e32 v144, v144
	v_exp_f32_e32 v145, v145
	s_waitcnt lgkmcnt(4)
	v_mfma_f32_32x32x16_bf16 v[0:15], v[172:175], v[188:191], v[0:15]
	v_exp_f32_e32 v146, v146
	v_exp_f32_e32 v147, v147
	v_add_f32_e32 v255, v144, v145
	v_add_f32_e32 v255, v255, v146
	v_add_f32_e32 v255, v255, v147
	s_waitcnt lgkmcnt(2)
	v_mfma_f32_32x32x16_bf16 v[160:175], v[196:199], v[192:195], 0
	v_cvt_pk_bf16_f32 v134, v140, v141
	v_cvt_pk_bf16_f32 v135, v142, v143
	v_sub_f32_e32 v148, v148, v229
	v_sub_f32_e32 v149, v149, v229
	v_sub_f32_e32 v150, v150, v229
	s_waitcnt lgkmcnt(1)
	v_mfma_f32_32x32x16_bf16 v[176:191], v[200:203], v[192:195], 0
	v_add3_u32 v230, v237, v241, s51
	ds_read_b128 v[196:199], v230
	ds_read_b128 v[200:203], v230 offset:8192
	v_add_u32_e32 v230, v236, v242
	ds_read_b128 v[192:195], v230
	v_sub_f32_e32 v151, v151, v229
	v_exp_f32_e32 v148, v148
	v_exp_f32_e32 v149, v149
	v_exp_f32_e32 v150, v150
	v_exp_f32_e32 v151, v151
	s_waitcnt lgkmcnt(2)
	v_mfma_f32_32x32x16_bf16 v[160:175], v[196:199], v[204:207], v[160:175]
	v_add_f32_e32 v255, v255, v148
	v_add_f32_e32 v255, v255, v149
	v_add_f32_e32 v255, v255, v150
	v_add_f32_e32 v255, v255, v151
	v_cvt_pk_bf16_f32 v136, v144, v145
	s_waitcnt lgkmcnt(1)
	v_mfma_f32_32x32x16_bf16 v[176:191], v[200:203], v[204:207], v[176:191]
	v_add3_u32 v230, v237, v242, s51
	ds_read_b128 v[196:199], v230
	ds_read_b128 v[200:203], v230 offset:8192
	v_add_u32_e32 v230, v236, v243
	ds_read_b128 v[204:207], v230
	v_cvt_pk_bf16_f32 v137, v146, v147
	v_sub_f32_e32 v152, v152, v229
	v_sub_f32_e32 v153, v153, v229
	v_sub_f32_e32 v154, v154, v229
	v_sub_f32_e32 v155, v155, v229
	s_waitcnt lgkmcnt(2)
	v_mfma_f32_32x32x16_bf16 v[160:175], v[196:199], v[192:195], v[160:175]
	v_exp_f32_e32 v152, v152
	v_exp_f32_e32 v153, v153
	v_exp_f32_e32 v154, v154
	v_exp_f32_e32 v155, v155
	v_add_f32_e32 v255, v255, v152
	s_waitcnt lgkmcnt(1)
	v_mfma_f32_32x32x16_bf16 v[176:191], v[200:203], v[192:195], v[176:191]
	v_add3_u32 v230, v237, v243, s51
	ds_read_b128 v[196:199], v230
	ds_read_b128 v[200:203], v230 offset:8192
	v_add_f32_e32 v255, v255, v153
	v_add_f32_e32 v255, v255, v154
	v_add_f32_e32 v255, v255, v155
	v_cvt_pk_bf16_f32 v138, v148, v149
	v_cvt_pk_bf16_f32 v139, v150, v151
	s_waitcnt lgkmcnt(1)
	v_mfma_f32_32x32x16_bf16 v[160:175], v[196:199], v[204:207], v[160:175]
	v_sub_f32_e32 v156, v156, v229
	v_sub_f32_e32 v157, v157, v229
	v_sub_f32_e32 v158, v158, v229
	v_sub_f32_e32 v159, v159, v229
	v_exp_f32_e32 v156, v156
	s_waitcnt lgkmcnt(0)
	v_mfma_f32_32x32x16_bf16 v[176:191], v[200:203], v[204:207], v[176:191]
	v_exp_f32_e32 v157, v157
	v_exp_f32_e32 v158, v158
	v_exp_f32_e32 v159, v159
	v_add_f32_e32 v255, v255, v156
	v_add_f32_e32 v255, v255, v157
	v_add_f32_e32 v255, v255, v158
	v_add_f32_e32 v255, v255, v159
	v_cvt_pk_bf16_f32 v140, v152, v153
	v_cvt_pk_bf16_f32 v141, v154, v155
	v_cvt_pk_bf16_f32 v142, v156, v157
	v_cvt_pk_bf16_f32 v143, v158, v159
	v_add_f32_e32 v254, v254, v255
	v_mov_b32_e32 v255, v254
	s_nop 1
	v_permlane32_swap_b32_e32 v254, v255
	v_add_f32_e32 v254, v254, v255
	v_fma_f32 v208, v208, v228, v254
	s_branch .Lattn_tail
